# g21: g17 + P8 final output stored non-temporal + mixer sum-of-squares lane reductions via DPP quad_perm adds instead of ds_bpermute
# baseline (speedup 1.0000x reference)
.Lvmk_ssd_done:
	v_lshlrev_b32_e32 v75, 16, v6
	v_and_b32_e32 v125, 0xffff0000, v5
	v_lshl_add_u32 v74, s48, 7, v209
	s_waitcnt lgkmcnt(0)
	v_lshlrev_b32_e32 v68, 16, v66
	v_and_b32_e32 v66, 0xffff0000, v66
	v_lshlrev_b32_e32 v69, 16, v67
	v_and_b32_e32 v67, 0xffff0000, v67
	v_fma_f32 v66, v135, v66, v95
	v_fma_f32 v68, v135, v68, v94
	ds_write_b32 v204, v66 offset:272
	v_fma_f32 v66, v135, v69, v96
	v_fmac_f32_e32 v97, v135, v67
	ds_write_b32 v204, v68
	ds_write_b32 v204, v66 offset:544
	ds_write_b32 v204, v97 offset:816
	ds_read_b64 v[66:67], v188
	v_and_b32_e32 v94, 0xffff0000, v3
	v_lshlrev_b32_e32 v95, 16, v4
	v_and_b32_e32 v96, 0xffff0000, v4
	v_lshlrev_b32_e32 v97, 16, v5
	s_waitcnt lgkmcnt(0)
	v_lshlrev_b32_e32 v68, 16, v66
	v_and_b32_e32 v66, 0xffff0000, v66
	v_lshlrev_b32_e32 v69, 16, v67
	v_and_b32_e32 v67, 0xffff0000, v67
	v_fma_f32 v66, v135, v66, v91
	v_fma_f32 v68, v135, v68, v90
	ds_write_b32 v204, v66 offset:336
	v_fma_f32 v66, v135, v69, v92
	v_fmac_f32_e32 v93, v135, v67
	ds_write_b32 v204, v68 offset:64
	ds_write_b32 v204, v66 offset:608
	ds_write_b32 v204, v93 offset:880
	ds_read_b64 v[66:67], v189
	v_and_b32_e32 v90, 0xffff0000, v9
	v_lshlrev_b32_e32 v91, 16, v2
	v_and_b32_e32 v92, 0xffff0000, v2
	v_lshlrev_b32_e32 v93, 16, v3
	s_waitcnt lgkmcnt(0)
	v_lshlrev_b32_e32 v68, 16, v66
	v_and_b32_e32 v66, 0xffff0000, v66
	v_lshlrev_b32_e32 v69, 16, v67
	v_and_b32_e32 v67, 0xffff0000, v67
	v_fma_f32 v66, v135, v66, v87
	v_fma_f32 v68, v135, v68, v86
	ds_write_b32 v204, v66 offset:400
	v_fma_f32 v66, v135, v69, v88
	v_fmac_f32_e32 v89, v135, v67
	ds_write_b32 v204, v68 offset:128
	ds_write_b32 v204, v66 offset:672
	ds_write_b32 v204, v89 offset:944
	ds_read_b64 v[66:67], v190
	v_and_b32_e32 v86, 0xffff0000, v7
	v_lshlrev_b32_e32 v87, 16, v8
	v_and_b32_e32 v88, 0xffff0000, v8
	v_lshlrev_b32_e32 v89, 16, v9
	s_waitcnt lgkmcnt(0)
	v_lshlrev_b32_e32 v68, 16, v66
	v_and_b32_e32 v66, 0xffff0000, v66
	v_lshlrev_b32_e32 v69, 16, v67
	v_and_b32_e32 v67, 0xffff0000, v67
	v_fma_f32 v66, v135, v66, v83
	v_fma_f32 v68, v135, v68, v82
	ds_write_b32 v204, v66 offset:464
	v_fma_f32 v66, v135, v69, v84
	v_fmac_f32_e32 v85, v135, v67
	ds_write_b32 v204, v68 offset:192
	ds_write_b32 v204, v66 offset:736
	ds_write_b32 v204, v85 offset:1008
	ds_read_b128 v[76:79], v205
	ds_read_b128 v[80:83], v205 offset:16
	ds_read_b128 v[70:73], v205 offset:32
	ds_read_b128 v[66:69], v205 offset:48
	v_and_b32_e32 v84, 0xffff0000, v6
	v_lshlrev_b32_e32 v85, 16, v7
	s_waitcnt lgkmcnt(0)
	v_mul_f32_e32 v76, v76, v75
	v_mul_f32_e32 v77, v77, v84
	v_mul_f32_e32 v78, v78, v85
	v_mul_f32_e32 v79, v79, v86
	v_mul_f32_e32 v80, v80, v87
	v_mul_f32_e32 v81, v81, v88
	v_mul_f32_e32 v82, v82, v89
	v_mul_f32_e32 v83, v83, v90
	v_mul_f32_e32 v70, v70, v91
	v_mul_f32_e32 v71, v71, v92
	v_mul_f32_e32 v72, v72, v93
	v_mul_f32_e32 v73, v73, v94
	v_mul_f32_e32 v66, v66, v95
	v_mul_f32_e32 v67, v67, v96
	v_mul_f32_e32 v68, v68, v97
	v_mul_f32_e32 v69, v69, v125
	v_mul_f32_e32 v75, 0xbfb8aa3b, v75
	v_mul_f32_e32 v84, 0xbfb8aa3b, v84
	v_mul_f32_e32 v85, 0xbfb8aa3b, v85
	v_mul_f32_e32 v86, 0xbfb8aa3b, v86
	v_mul_f32_e32 v87, 0xbfb8aa3b, v87
	v_mul_f32_e32 v88, 0xbfb8aa3b, v88
	v_mul_f32_e32 v89, 0xbfb8aa3b, v89
	v_mul_f32_e32 v90, 0xbfb8aa3b, v90
	v_mul_f32_e32 v91, 0xbfb8aa3b, v91
	v_mul_f32_e32 v92, 0xbfb8aa3b, v92
	v_mul_f32_e32 v93, 0xbfb8aa3b, v93
	v_mul_f32_e32 v94, 0xbfb8aa3b, v94
	v_mul_f32_e32 v95, 0xbfb8aa3b, v95
	v_mul_f32_e32 v96, 0xbfb8aa3b, v96
	v_mul_f32_e32 v97, 0xbfb8aa3b, v97
	v_mul_f32_e32 v125, 0xbfb8aa3b, v125
	v_exp_f32_e32 v75, v75
	v_exp_f32_e32 v84, v84
	v_exp_f32_e32 v85, v85
	v_exp_f32_e32 v86, v86
	v_exp_f32_e32 v87, v87
	v_exp_f32_e32 v88, v88
	v_exp_f32_e32 v89, v89
	v_exp_f32_e32 v90, v90
	v_exp_f32_e32 v91, v91
	v_exp_f32_e32 v92, v92
	v_exp_f32_e32 v93, v93
	v_exp_f32_e32 v94, v94
	v_exp_f32_e32 v95, v95
	v_exp_f32_e32 v96, v96
	v_exp_f32_e32 v97, v97
	v_exp_f32_e32 v125, v125
	v_add_f32_e32 v75, 1.0, v75
	v_add_f32_e32 v84, 1.0, v84
	v_add_f32_e32 v85, 1.0, v85
	v_add_f32_e32 v86, 1.0, v86
	v_add_f32_e32 v87, 1.0, v87
	v_add_f32_e32 v88, 1.0, v88
	v_add_f32_e32 v89, 1.0, v89
	v_add_f32_e32 v90, 1.0, v90
	v_add_f32_e32 v91, 1.0, v91
	v_add_f32_e32 v92, 1.0, v92
	v_add_f32_e32 v93, 1.0, v93
	v_add_f32_e32 v94, 1.0, v94
	v_add_f32_e32 v95, 1.0, v95
	v_add_f32_e32 v96, 1.0, v96
	v_add_f32_e32 v97, 1.0, v97
	v_add_f32_e32 v125, 1.0, v125
	v_rcp_f32_e32 v75, v75
	v_rcp_f32_e32 v84, v84
	v_rcp_f32_e32 v85, v85
	v_rcp_f32_e32 v86, v86
	v_rcp_f32_e32 v87, v87
	v_rcp_f32_e32 v88, v88
	v_rcp_f32_e32 v89, v89
	v_rcp_f32_e32 v90, v90
	v_rcp_f32_e32 v91, v91
	v_rcp_f32_e32 v92, v92
	v_rcp_f32_e32 v93, v93
	v_rcp_f32_e32 v94, v94
	v_rcp_f32_e32 v95, v95
	v_rcp_f32_e32 v96, v96
	v_rcp_f32_e32 v97, v97
	v_rcp_f32_e32 v125, v125
	v_mul_f32_e32 v76, v75, v76
	v_mul_f32_e32 v77, v84, v77
	v_mul_f32_e32 v78, v85, v78
	v_mul_f32_e32 v79, v86, v79
	v_mul_f32_e32 v80, v87, v80
	v_mul_f32_e32 v81, v88, v81
	v_mul_f32_e32 v82, v89, v82
	v_mul_f32_e32 v83, v90, v83
	v_mul_f32_e32 v70, v91, v70
	v_mul_f32_e32 v71, v92, v71
	v_mul_f32_e32 v72, v93, v72
	v_mul_f32_e32 v73, v94, v73
	v_mul_f32_e32 v84, v95, v66
	v_mul_f32_e32 v85, v96, v67
	v_mul_f32_e32 v68, v97, v68
	v_mul_f32_e32 v69, v125, v69
	v_mul_f32_e32 v86, v77, v77
	v_fmac_f32_e32 v86, v76, v76
	v_fmac_f32_e32 v86, v78, v78
	v_fmac_f32_e32 v86, v79, v79
	v_fmac_f32_e32 v86, v80, v80
	v_fmac_f32_e32 v86, v81, v81
	v_fmac_f32_e32 v86, v82, v82
	v_fmac_f32_e32 v86, v83, v83
	v_fmac_f32_e32 v86, v70, v70
	v_fmac_f32_e32 v86, v71, v71
	v_fmac_f32_e32 v86, v72, v72
	v_fmac_f32_e32 v86, v73, v73
	v_fmac_f32_e32 v86, v84, v84
	v_fmac_f32_e32 v86, v85, v85
	v_fmac_f32_e32 v86, v68, v68
	v_ashrrev_i32_e32 v75, 31, v74
	v_xor_b32_e32 v87, 1, v99
	v_and_b32_e32 v66, 64, v99
	v_add_u32_e32 v67, 64, v66
	v_cmp_lt_i32_e32 vcc, v87, v67
	v_fmac_f32_e32 v86, v69, v69
	s_nop 0
	v_cndmask_b32_e32 v87, v99, v87, vcc
	v_lshlrev_b32_e32 v212, 2, v87
	v_add_f32_dpp v86, v86, v86 quad_perm:[1,0,3,2] row_mask:0xf bank_mask:0xf
	v_xor_b32_e32 v87, 2, v99
	v_cmp_lt_i32_e32 vcc, v87, v67
	s_nop 1
	v_cndmask_b32_e32 v87, v99, v87, vcc
	v_lshlrev_b32_e32 v213, 2, v87
	v_add_f32_dpp v86, v86, v86 quad_perm:[2,3,0,1] row_mask:0xf bank_mask:0xf
	s_and_saveexec_b64 s[0:1], s[26:27]
	s_cbranch_execz .LBB0_234
	v_lshlrev_b64 v[88:89], 7, v[74:75]
	v_lshl_add_u64 v[88:89], s[38:39], 0, v[88:89]
	global_store_dword v[88:89], v86, off

.LBB0_270:
	s_or_b64 exec, exec, s[0:1]
	s_waitcnt lgkmcnt(0)
	ds_read_b128 v[66:69], v180
	ds_read_b128 v[70:73], v180 offset:64
	ds_read_b128 v[78:81], v125 offset:2560
	s_waitcnt lgkmcnt(1)
	v_fma_f32 v66, v74, v70, v66
	s_waitcnt lgkmcnt(0)
	v_max_f32_e32 v70, v78, v78
	v_max_f32_e64 v66, |v66|, v70
	v_rcp_f32_e32 v66, v66
	v_fma_f32 v67, v75, v71, v67
	v_max_f32_e32 v70, v79, v79
	v_max_f32_e64 v67, |v67|, v70
	v_rcp_f32_e32 v67, v67
	v_mul_f32_e32 v70, v86, v66
	v_mul_f32_e32 v71, v90, v66
	ds_write2_b32 v204, v70, v71 offset1:16
	v_mul_f32_e32 v70, v94, v66
	v_mul_f32_e32 v66, v98, v66
	ds_write2_b32 v204, v70, v66 offset0:32 offset1:48
	v_mul_f32_e32 v66, v87, v67
	v_mul_f32_e32 v70, v91, v67
	ds_write2_b32 v204, v66, v70 offset0:68 offset1:84
	v_fma_f32 v66, v76, v72, v68
	v_max_f32_e32 v68, v80, v80
	v_max_f32_e64 v66, |v66|, v68
	v_rcp_f32_e32 v66, v66
	v_mul_f32_e32 v68, v95, v67
	v_mul_f32_e32 v67, v99, v67
	ds_write2_b32 v204, v68, v67 offset0:100 offset1:116
	v_mul_f32_e32 v67, v88, v66
	v_mul_f32_e32 v68, v92, v66
	ds_write2_b32 v204, v67, v68 offset0:136 offset1:152
	v_fmac_f32_e32 v69, v77, v73
	v_max_f32_e32 v67, v81, v81
	v_max_f32_e64 v67, |v69|, v67
	v_rcp_f32_e32 v67, v67
	v_mul_f32_e32 v68, v96, v66
	v_mul_f32_e32 v66, v100, v66
	ds_write2_b32 v204, v68, v66 offset0:168 offset1:184
	v_mul_f32_e32 v66, v89, v67
	v_mul_f32_e32 v68, v93, v67
	ds_write2_b32 v204, v66, v68 offset0:204 offset1:220
	v_mul_f32_e32 v66, v97, v67
	v_mul_f32_e32 v67, v101, v67
	ds_write2_b32 v204, v66, v67 offset0:236 offset1:252
	ds_read_b128 v[78:81], v205
	ds_read_b128 v[74:77], v205 offset:16
	ds_read_b128 v[70:73], v205 offset:32
	ds_read_b128 v[66:69], v205 offset:48
	s_waitcnt lgkmcnt(3)
	v_mul_f32_e32 v82, v79, v79
	v_fmac_f32_e32 v82, v78, v78
	v_fmac_f32_e32 v82, v80, v80
	v_fmac_f32_e32 v82, v81, v81
	s_waitcnt lgkmcnt(2)
	v_fmac_f32_e32 v82, v74, v74
	v_fmac_f32_e32 v82, v75, v75
	v_fmac_f32_e32 v82, v76, v76
	v_fmac_f32_e32 v82, v77, v77
	s_waitcnt lgkmcnt(1)
	v_fmac_f32_e32 v82, v70, v70
	v_fmac_f32_e32 v82, v71, v71
	v_fmac_f32_e32 v82, v72, v72
	v_fmac_f32_e32 v82, v73, v73
	s_waitcnt lgkmcnt(0)
	v_fmac_f32_e32 v82, v66, v66
	v_fmac_f32_e32 v82, v67, v67
	v_fmac_f32_e32 v82, v68, v68
	v_fmac_f32_e32 v82, v69, v69
	s_nop 1
	v_add_f32_dpp v84, v82, v82 quad_perm:[1,0,3,2] row_mask:0xf bank_mask:0xf
	s_nop 1
	v_add_f32_dpp v84, v84, v84 quad_perm:[2,3,0,1] row_mask:0xf bank_mask:0xf
	v_lshl_add_u32 v82, s90, 7, v209
	v_ashrrev_i32_e32 v83, 31, v82
	s_and_saveexec_b64 s[0:1], s[26:27]
	s_cbranch_execz .LBB0_272
	v_lshlrev_b64 v[86:87], 7, v[82:83]
	v_lshl_add_u64 v[86:87], s[36:37], 0, v[86:87]
	global_store_dword v[86:87], v84, off

.LBB0_786:
	s_or_b64 exec, exec, s[2:3]
	ds_bpermute_b32 v28, v16, v14
	ds_bpermute_b32 v30, v17, v14
	s_add_i32 s4, s4, s6
	s_cmpk_lt_i32 s4, 0x4000
	v_lshl_add_u64 v[12:13], v[12:13], 0, s[12:13]
	s_waitcnt lgkmcnt(1)
	v_ashrrev_i32_e32 v29, 31, v28
	v_lshlrev_b64 v[28:29], 11, v[28:29]
	v_lshl_add_u64 v[28:29], v[6:7], 0, v[28:29]
	s_waitcnt lgkmcnt(0)
	v_ashrrev_i32_e32 v31, 31, v30
	global_load_dwordx2 v[44:45], v[28:29], off
	global_load_dwordx2 v[46:47], v[28:29], off offset:512
	global_load_dwordx2 v[48:49], v[28:29], off offset:1024
	global_load_dwordx2 v[50:51], v[28:29], off offset:1536
	v_lshlrev_b64 v[28:29], 11, v[30:31]
	ds_bpermute_b32 v30, v18, v14
	ds_bpermute_b32 v14, v19, v14
	v_lshl_add_u64 v[28:29], v[6:7], 0, v[28:29]
	global_load_dwordx2 v[52:53], v[28:29], off
	global_load_dwordx2 v[54:55], v[28:29], off offset:512
	global_load_dwordx2 v[56:57], v[28:29], off offset:1024
	global_load_dwordx2 v[58:59], v[28:29], off offset:1536
	s_waitcnt lgkmcnt(1)
	v_ashrrev_i32_e32 v31, 31, v30
	v_lshlrev_b64 v[28:29], 11, v[30:31]
	v_lshl_add_u64 v[28:29], v[6:7], 0, v[28:29]
	global_load_dwordx2 v[60:61], v[28:29], off
	global_load_dwordx2 v[62:63], v[28:29], off offset:512
	global_load_dwordx2 v[64:65], v[28:29], off offset:1024
	global_load_dwordx2 v[66:67], v[28:29], off offset:1536
	s_waitcnt lgkmcnt(0)
	v_ashrrev_i32_e32 v15, 31, v14
	v_lshl_add_u64 v[28:29], s[96:97], 0, v[8:9]
	v_lshlrev_b64 v[14:15], 11, v[14:15]
	v_add_co_u32_e32 v74, vcc, 0x56800000, v28
	v_lshl_add_u64 v[14:15], v[6:7], 0, v[14:15]
	s_nop 0
	v_addc_co_u32_e32 v75, vcc, 0, v29, vcc
	global_load_dwordx2 v[68:69], v[14:15], off
	global_load_dwordx2 v[70:71], v[14:15], off offset:512
	global_load_dwordx2 v[72:73], v[14:15], off offset:1024
	v_lshl_add_u64 v[8:9], v[8:9], 0, s[8:9]
	global_load_dwordx2 v[14:15], v[14:15], off offset:1536
	s_nop 0
	global_load_dwordx4 v[28:31], v[74:75], off offset:3072
	global_load_dwordx4 v[32:35], v[74:75], off
	global_load_dwordx4 v[36:39], v[74:75], off offset:2048
	global_load_dwordx4 v[40:43], v[74:75], off offset:1024
	s_waitcnt vmcnt(19)
	v_cvt_pk_f32_fp8_e32 v[74:75], v44
	v_cvt_pk_f32_fp8_sdwa v[76:77], v44 src0_sel:WORD_1
	s_waitcnt vmcnt(18)
	v_cvt_pk_f32_fp8_e32 v[82:83], v46
	v_cvt_pk_f32_fp8_sdwa v[84:85], v46 src0_sel:WORD_1
	v_cvt_pk_f32_fp8_e32 v[86:87], v47
	v_cvt_pk_f32_fp8_sdwa v[88:89], v47 src0_sel:WORD_1
	s_waitcnt vmcnt(15)
	v_cvt_pk_f32_fp8_e32 v[104:105], v52
	v_cvt_pk_f32_fp8_sdwa v[106:107], v52 src0_sel:WORD_1
	s_waitcnt vmcnt(12)
	v_cvt_pk_f32_fp8_e32 v[122:123], v58
	v_cvt_pk_f32_fp8_sdwa v[124:125], v58 src0_sel:WORD_1
	v_cvt_pk_f32_fp8_e32 v[126:127], v59
	v_cvt_pk_f32_fp8_sdwa v[46:47], v59 src0_sel:WORD_1
	s_waitcnt vmcnt(11)
	v_cvt_pk_f32_fp8_e32 v[58:59], v60
	v_cvt_pk_f32_fp8_e32 v[78:79], v45
	v_cvt_pk_f32_fp8_e32 v[90:91], v48
	v_cvt_pk_f32_fp8_sdwa v[92:93], v48 src0_sel:WORD_1
	v_cvt_pk_f32_fp8_e32 v[94:95], v49
	v_cvt_pk_f32_fp8_sdwa v[96:97], v49 src0_sel:WORD_1
	v_cvt_pk_f32_fp8_sdwa v[128:129], v60 src0_sel:WORD_1
	s_waitcnt vmcnt(8)
	v_cvt_pk_f32_fp8_e32 v[144:145], v66
	v_cvt_pk_f32_fp8_sdwa v[146:147], v66 src0_sel:WORD_1
	v_cvt_pk_f32_fp8_e32 v[148:149], v67
	v_cvt_pk_f32_fp8_sdwa v[48:49], v67 src0_sel:WORD_1
	s_waitcnt vmcnt(7)
	v_cvt_pk_f32_fp8_e32 v[66:67], v68
	s_waitcnt vmcnt(2)
	v_lshlrev_b32_e32 v174, 16, v32
	v_and_b32_e32 v175, 0xffff0000, v32
	v_cvt_pk_f32_fp8_sdwa v[80:81], v45 src0_sel:WORD_1
	v_cvt_pk_f32_fp8_e32 v[108:109], v53
	v_cvt_pk_f32_fp8_sdwa v[150:151], v68 src0_sel:WORD_1
	v_pk_fma_f32 v[74:75], v[74:75], s[14:15], v[174:175] op_sel_hi:[1,0,1]
	v_lshlrev_b32_e32 v32, 16, v33
	v_and_b32_e32 v33, 0xffff0000, v33
	v_cvt_pk_f32_fp8_sdwa v[52:53], v53 src0_sel:WORD_1
	v_cvt_pk_f32_fp8_e32 v[130:131], v61
	v_pk_fma_f32 v[74:75], v[104:105], s[14:15], v[74:75] op_sel_hi:[1,0,1]
	v_pk_fma_f32 v[32:33], v[76:77], s[14:15], v[32:33] op_sel_hi:[1,0,1]
	v_cvt_pk_f32_fp8_sdwa v[60:61], v61 src0_sel:WORD_1
	v_cvt_pk_f32_fp8_e32 v[152:153], v69
	v_pk_fma_f32 v[58:59], v[58:59], s[14:15], v[74:75] op_sel_hi:[1,0,1]
	v_pk_fma_f32 v[32:33], v[106:107], s[14:15], v[32:33] op_sel_hi:[1,0,1]
	v_lshlrev_b32_e32 v76, 16, v34
	v_and_b32_e32 v77, 0xffff0000, v34
	v_pk_fma_f32 v[58:59], v[66:67], s[14:15], v[58:59] op_sel_hi:[1,0,1]
	v_pk_fma_f32 v[32:33], v[128:129], s[14:15], v[32:33] op_sel_hi:[1,0,1]
	v_pk_fma_f32 v[76:77], v[78:79], s[14:15], v[76:77] op_sel_hi:[1,0,1]
	v_lshlrev_b32_e32 v34, 16, v35
	v_and_b32_e32 v35, 0xffff0000, v35
	v_cvt_pk_f32_fp8_e32 v[110:111], v54
	v_cvt_pk_f32_fp8_sdwa v[68:69], v69 src0_sel:WORD_1
	v_pk_mul_f32 v[66:67], v[58:59], v[58:59]
	v_pk_fma_f32 v[32:33], v[150:151], s[14:15], v[32:33] op_sel_hi:[1,0,1]
	v_pk_fma_f32 v[76:77], v[108:109], s[14:15], v[76:77] op_sel_hi:[1,0,1]
	v_pk_fma_f32 v[34:35], v[80:81], s[14:15], v[34:35] op_sel_hi:[1,0,1]
	v_cvt_pk_f32_fp8_e32 v[132:133], v62
	v_pk_mul_f32 v[74:75], v[32:33], v[32:33]
	v_pk_fma_f32 v[76:77], v[130:131], s[14:15], v[76:77] op_sel_hi:[1,0,1]
	v_pk_fma_f32 v[34:35], v[52:53], s[14:15], v[34:35] op_sel_hi:[1,0,1]
	v_add_f32_e32 v66, v66, v67
	v_cvt_pk_f32_fp8_sdwa v[112:113], v54 src0_sel:WORD_1
	v_cvt_pk_f32_fp8_e32 v[154:155], v70
	v_pk_fma_f32 v[76:77], v[152:153], s[14:15], v[76:77] op_sel_hi:[1,0,1]
	v_pk_fma_f32 v[34:35], v[60:61], s[14:15], v[34:35] op_sel_hi:[1,0,1]
	s_waitcnt vmcnt(0)
	v_lshlrev_b32_e32 v60, 16, v40
	v_and_b32_e32 v61, 0xffff0000, v40
	v_add_f32_e32 v66, v66, v74
	v_cvt_pk_f32_fp8_sdwa v[134:135], v62 src0_sel:WORD_1
	v_pk_mul_f32 v[78:79], v[76:77], v[76:77]
	v_pk_fma_f32 v[60:61], v[82:83], s[14:15], v[60:61] op_sel_hi:[1,0,1]
	v_add_f32_e32 v66, v75, v66
	v_cvt_pk_f32_fp8_e32 v[114:115], v55
	v_cvt_pk_f32_fp8_sdwa v[156:157], v70 src0_sel:WORD_1
	v_pk_fma_f32 v[34:35], v[68:69], s[14:15], v[34:35] op_sel_hi:[1,0,1]
	v_pk_fma_f32 v[60:61], v[110:111], s[14:15], v[60:61] op_sel_hi:[1,0,1]
	v_lshlrev_b32_e32 v40, 16, v41
	v_and_b32_e32 v41, 0xffff0000, v41
	v_add_f32_e32 v66, v78, v66
	v_cvt_pk_f32_fp8_sdwa v[54:55], v55 src0_sel:WORD_1
	v_cvt_pk_f32_fp8_e32 v[136:137], v63
	v_pk_mul_f32 v[52:53], v[34:35], v[34:35]
	v_pk_fma_f32 v[60:61], v[132:133], s[14:15], v[60:61] op_sel_hi:[1,0,1]
	v_pk_fma_f32 v[40:41], v[84:85], s[14:15], v[40:41] op_sel_hi:[1,0,1]
	v_add_f32_e32 v66, v79, v66
	v_cvt_pk_f32_fp8_sdwa v[62:63], v63 src0_sel:WORD_1
	v_cvt_pk_f32_fp8_e32 v[158:159], v71
	v_pk_fma_f32 v[60:61], v[154:155], s[14:15], v[60:61] op_sel_hi:[1,0,1]
	v_pk_fma_f32 v[40:41], v[112:113], s[14:15], v[40:41] op_sel_hi:[1,0,1]
	v_lshlrev_b32_e32 v82, 16, v42
	v_and_b32_e32 v83, 0xffff0000, v42
	v_add_f32_e32 v52, v52, v66
	v_pk_mul_f32 v[68:69], v[60:61], v[60:61]
	v_pk_fma_f32 v[40:41], v[134:135], s[14:15], v[40:41] op_sel_hi:[1,0,1]
	v_pk_fma_f32 v[82:83], v[86:87], s[14:15], v[82:83] op_sel_hi:[1,0,1]
	v_lshlrev_b32_e32 v42, 16, v43
	v_and_b32_e32 v43, 0xffff0000, v43
	v_add_f32_e32 v52, v53, v52
	v_cvt_pk_f32_fp8_e32 v[116:117], v56
	v_cvt_pk_f32_fp8_sdwa v[70:71], v71 src0_sel:WORD_1
	v_pk_fma_f32 v[40:41], v[156:157], s[14:15], v[40:41] op_sel_hi:[1,0,1]
	v_pk_fma_f32 v[82:83], v[114:115], s[14:15], v[82:83] op_sel_hi:[1,0,1]
	v_pk_fma_f32 v[42:43], v[88:89], s[14:15], v[42:43] op_sel_hi:[1,0,1]
	v_add_f32_e32 v52, v68, v52
	v_cvt_pk_f32_fp8_e32 v[138:139], v64
	v_pk_mul_f32 v[80:81], v[40:41], v[40:41]
	v_pk_fma_f32 v[82:83], v[136:137], s[14:15], v[82:83] op_sel_hi:[1,0,1]
	v_pk_fma_f32 v[42:43], v[54:55], s[14:15], v[42:43] op_sel_hi:[1,0,1]
	v_add_f32_e32 v52, v69, v52
	v_cvt_pk_f32_fp8_sdwa v[118:119], v56 src0_sel:WORD_1
	v_cvt_pk_f32_fp8_e32 v[160:161], v72
	v_pk_fma_f32 v[82:83], v[158:159], s[14:15], v[82:83] op_sel_hi:[1,0,1]
	v_pk_fma_f32 v[42:43], v[62:63], s[14:15], v[42:43] op_sel_hi:[1,0,1]
	v_lshlrev_b32_e32 v62, 16, v36
	v_and_b32_e32 v63, 0xffff0000, v36
	v_add_f32_e32 v52, v80, v52
	v_cvt_pk_f32_fp8_sdwa v[44:45], v51 src0_sel:WORD_1
	v_cvt_pk_f32_fp8_sdwa v[140:141], v64 src0_sel:WORD_1
	v_pk_mul_f32 v[84:85], v[82:83], v[82:83]
	v_pk_fma_f32 v[62:63], v[90:91], s[14:15], v[62:63] op_sel_hi:[1,0,1]
	v_add_f32_e32 v52, v81, v52
	v_cvt_pk_f32_fp8_e32 v[120:121], v57
	v_cvt_pk_f32_fp8_sdwa v[162:163], v72 src0_sel:WORD_1
	v_pk_fma_f32 v[42:43], v[70:71], s[14:15], v[42:43] op_sel_hi:[1,0,1]
	v_pk_fma_f32 v[62:63], v[116:117], s[14:15], v[62:63] op_sel_hi:[1,0,1]
	v_lshlrev_b32_e32 v36, 16, v37
	v_and_b32_e32 v37, 0xffff0000, v37
	v_add_f32_e32 v52, v84, v52
	v_cvt_pk_f32_fp8_sdwa v[56:57], v57 src0_sel:WORD_1
	v_cvt_pk_f32_fp8_e32 v[142:143], v65
	v_pk_mul_f32 v[54:55], v[42:43], v[42:43]
	v_pk_fma_f32 v[62:63], v[138:139], s[14:15], v[62:63] op_sel_hi:[1,0,1]
	v_pk_fma_f32 v[36:37], v[92:93], s[14:15], v[36:37] op_sel_hi:[1,0,1]
	v_add_f32_e32 v52, v85, v52
	v_cvt_pk_f32_fp8_e32 v[98:99], v50
	v_cvt_pk_f32_fp8_sdwa v[100:101], v50 src0_sel:WORD_1
	v_cvt_pk_f32_fp8_e32 v[102:103], v51
	v_cvt_pk_f32_fp8_sdwa v[64:65], v65 src0_sel:WORD_1
	v_cvt_pk_f32_fp8_e32 v[164:165], v73
	v_cvt_pk_f32_fp8_e32 v[166:167], v14
	v_cvt_pk_f32_fp8_sdwa v[168:169], v14 src0_sel:WORD_1
	v_cvt_pk_f32_fp8_e32 v[170:171], v15
	v_cvt_pk_f32_fp8_sdwa v[14:15], v15 src0_sel:WORD_1
	v_and_b32_e32 v51, 0xffff0000, v31
	v_lshlrev_b32_e32 v50, 16, v31
	v_pk_fma_f32 v[62:63], v[160:161], s[14:15], v[62:63] op_sel_hi:[1,0,1]
	v_pk_fma_f32 v[36:37], v[118:119], s[14:15], v[36:37] op_sel_hi:[1,0,1]
	v_lshlrev_b32_e32 v88, 16, v38
	v_and_b32_e32 v89, 0xffff0000, v38
	v_add_f32_e32 v52, v54, v52
	v_pk_fma_f32 v[44:45], v[44:45], s[14:15], v[50:51] op_sel_hi:[1,0,1]
	v_pk_mul_f32 v[70:71], v[62:63], v[62:63]
	v_pk_fma_f32 v[36:37], v[140:141], s[14:15], v[36:37] op_sel_hi:[1,0,1]
	v_pk_fma_f32 v[88:89], v[94:95], s[14:15], v[88:89] op_sel_hi:[1,0,1]
	v_lshlrev_b32_e32 v38, 16, v39
	v_and_b32_e32 v39, 0xffff0000, v39
	v_add_f32_e32 v52, v55, v52
	v_cvt_pk_f32_fp8_sdwa v[72:73], v73 src0_sel:WORD_1
	v_pk_fma_f32 v[44:45], v[46:47], s[14:15], v[44:45] op_sel_hi:[1,0,1]
	v_pk_fma_f32 v[36:37], v[162:163], s[14:15], v[36:37] op_sel_hi:[1,0,1]
	v_pk_fma_f32 v[88:89], v[120:121], s[14:15], v[88:89] op_sel_hi:[1,0,1]
	v_pk_fma_f32 v[38:39], v[96:97], s[14:15], v[38:39] op_sel_hi:[1,0,1]
	v_add_f32_e32 v52, v70, v52
	v_pk_fma_f32 v[44:45], v[48:49], s[14:15], v[44:45] op_sel_hi:[1,0,1]
	v_pk_mul_f32 v[86:87], v[36:37], v[36:37]
	v_pk_fma_f32 v[88:89], v[142:143], s[14:15], v[88:89] op_sel_hi:[1,0,1]
	v_pk_fma_f32 v[38:39], v[56:57], s[14:15], v[38:39] op_sel_hi:[1,0,1]
	v_add_f32_e32 v52, v71, v52
	v_pk_fma_f32 v[14:15], v[14:15], s[14:15], v[44:45] op_sel_hi:[1,0,1]
	global_load_dwordx4 v[44:47], v[0:1], off offset:16
	global_load_dwordx4 v[48:51], v[0:1], off
	v_pk_fma_f32 v[88:89], v[164:165], s[14:15], v[88:89] op_sel_hi:[1,0,1]
	v_pk_fma_f32 v[38:39], v[64:65], s[14:15], v[38:39] op_sel_hi:[1,0,1]
	v_lshlrev_b32_e32 v64, 16, v28
	v_and_b32_e32 v65, 0xffff0000, v28
	v_add_f32_e32 v52, v86, v52
	v_pk_mul_f32 v[90:91], v[88:89], v[88:89]
	v_pk_fma_f32 v[64:65], v[98:99], s[14:15], v[64:65] op_sel_hi:[1,0,1]
	v_add_f32_e32 v52, v87, v52
	v_pk_fma_f32 v[38:39], v[72:73], s[14:15], v[38:39] op_sel_hi:[1,0,1]
	v_pk_fma_f32 v[64:65], v[122:123], s[14:15], v[64:65] op_sel_hi:[1,0,1]
	v_lshlrev_b32_e32 v28, 16, v29
	v_and_b32_e32 v29, 0xffff0000, v29
	v_add_f32_e32 v52, v90, v52
	v_pk_mul_f32 v[56:57], v[38:39], v[38:39]
	v_pk_fma_f32 v[64:65], v[144:145], s[14:15], v[64:65] op_sel_hi:[1,0,1]
	v_pk_fma_f32 v[28:29], v[100:101], s[14:15], v[28:29] op_sel_hi:[1,0,1]
	v_add_f32_e32 v52, v91, v52
	v_pk_fma_f32 v[64:65], v[166:167], s[14:15], v[64:65] op_sel_hi:[1,0,1]
	v_pk_fma_f32 v[28:29], v[124:125], s[14:15], v[28:29] op_sel_hi:[1,0,1]
	v_lshlrev_b32_e32 v94, 16, v30
	v_and_b32_e32 v95, 0xffff0000, v30
	v_add_f32_e32 v52, v56, v52
	v_pk_mul_f32 v[72:73], v[64:65], v[64:65]
	v_pk_fma_f32 v[28:29], v[146:147], s[14:15], v[28:29] op_sel_hi:[1,0,1]
	v_pk_fma_f32 v[30:31], v[102:103], s[14:15], v[94:95] op_sel_hi:[1,0,1]
	v_add_f32_e32 v52, v57, v52
	v_pk_fma_f32 v[92:93], v[168:169], s[14:15], v[28:29] op_sel_hi:[1,0,1]
	v_pk_fma_f32 v[30:31], v[126:127], s[14:15], v[30:31] op_sel_hi:[1,0,1]
	v_add_f32_e32 v52, v72, v52
	v_pk_mul_f32 v[28:29], v[92:93], v[92:93]
	v_pk_fma_f32 v[30:31], v[148:149], s[14:15], v[30:31] op_sel_hi:[1,0,1]
	v_add_f32_e32 v52, v73, v52
	v_pk_fma_f32 v[94:95], v[170:171], s[14:15], v[30:31] op_sel_hi:[1,0,1]
	v_add_f32_e32 v28, v28, v52
	v_pk_mul_f32 v[30:31], v[94:95], v[94:95]
	v_add_f32_e32 v28, v29, v28
	v_add_f32_e32 v28, v30, v28
	v_pk_mul_f32 v[172:173], v[14:15], v[14:15]
	v_add_f32_e32 v28, v31, v28
	v_add_f32_e32 v28, v172, v28
	v_add_f32_e32 v28, v173, v28
	ds_bpermute_b32 v29, v20, v28
	s_waitcnt lgkmcnt(0)
	v_add_f32_e32 v28, v28, v29
	ds_bpermute_b32 v29, v21, v28
	s_waitcnt lgkmcnt(0)
	v_add_f32_e32 v28, v28, v29
	ds_bpermute_b32 v29, v22, v28
	s_waitcnt lgkmcnt(0)
	v_add_f32_e32 v28, v28, v29
	ds_bpermute_b32 v29, v23, v28
	s_waitcnt lgkmcnt(0)
	v_add_f32_e32 v28, v28, v29
	ds_bpermute_b32 v29, v24, v28
	s_waitcnt lgkmcnt(0)
	v_add_f32_e32 v28, v28, v29
	ds_bpermute_b32 v29, v25, v28
	s_waitcnt lgkmcnt(0)
	v_add_f32_e32 v28, v28, v29
	v_fmamk_f32 v28, v28, 0x3a000000, v26
	v_mul_f32_e32 v29, 0x4f800000, v28
	v_cmp_gt_f32_e32 vcc, s5, v28
	s_nop 1
	v_cndmask_b32_e32 v28, v28, v29, vcc
	v_sqrt_f32_e32 v29, v28
	s_nop 0
	v_add_u32_e32 v30, -1, v29
	v_fma_f32 v31, -v30, v29, v28
	v_cmp_ge_f32_e64 s[2:3], 0, v31
	v_add_u32_e32 v31, 1, v29
	s_nop 0
	v_cndmask_b32_e64 v30, v29, v30, s[2:3]
	v_fma_f32 v29, -v31, v29, v28
	v_cmp_lt_f32_e64 s[2:3], 0, v29
	s_nop 1
	v_cndmask_b32_e64 v29, v30, v31, s[2:3]
	v_mul_f32_e32 v30, 0x37800000, v29
	v_cndmask_b32_e32 v29, v29, v30, vcc
	v_cmp_class_f32_e32 vcc, v28, v27
	s_nop 1
	v_cndmask_b32_e32 v28, v29, v28, vcc
	v_div_scale_f32 v29, s[2:3], v28, v28, 1.0
	v_rcp_f32_e32 v30, v29
	s_nop 0
	v_fma_f32 v31, -v29, v30, 1.0
	v_fmac_f32_e32 v30, v31, v30
	v_div_scale_f32 v31, vcc, 1.0, v28, 1.0
	v_mul_f32_e32 v52, v31, v30
	v_fma_f32 v53, -v29, v52, v31
	v_fmac_f32_e32 v52, v53, v30
	v_fma_f32 v29, -v29, v52, v31
	v_div_fmas_f32 v29, v29, v30, v52
	v_div_fixup_f32 v52, v29, v28, 1.0
	v_pk_mul_f32 v[28:29], v[58:59], v[52:53] op_sel_hi:[1,0]
	v_pk_mul_f32 v[30:31], v[32:33], v[52:53] op_sel_hi:[1,0]
	s_waitcnt vmcnt(0)
	v_pk_mul_f32 v[28:29], v[48:49], v[28:29]
	v_pk_mul_f32 v[30:31], v[50:51], v[30:31]
	global_store_dwordx4 v[10:11], v[28:31], off offset:-4096 nt
	v_pk_mul_f32 v[40:41], v[40:41], v[52:53] op_sel_hi:[1,0]
	v_pk_mul_f32 v[36:37], v[36:37], v[52:53] op_sel_hi:[1,0]
	v_pk_mul_f32 v[28:29], v[76:77], v[52:53] op_sel_hi:[1,0]
	v_pk_mul_f32 v[30:31], v[34:35], v[52:53] op_sel_hi:[1,0]
	v_pk_mul_f32 v[28:29], v[44:45], v[28:29]
	v_pk_mul_f32 v[30:31], v[46:47], v[30:31]
	global_store_dwordx4 v[10:11], v[28:31], off offset:-4080 nt
	global_load_dwordx4 v[28:31], v[0:1], off offset:2048
	s_nop 0
	global_load_dwordx4 v[32:35], v[0:1], off offset:2064
	v_pk_mul_f32 v[44:45], v[60:61], v[52:53] op_sel_hi:[1,0]
	v_pk_mul_f32 v[38:39], v[38:39], v[52:53] op_sel_hi:[1,0]
	v_pk_mul_f32 v[14:15], v[14:15], v[52:53] op_sel_hi:[1,0]
	s_waitcnt vmcnt(1)
	v_pk_mul_f32 v[28:29], v[28:29], v[44:45]
	v_pk_mul_f32 v[30:31], v[30:31], v[40:41]
	global_store_dwordx4 v[10:11], v[28:31], off offset:-2048 nt
	v_pk_mul_f32 v[40:41], v[62:63], v[52:53] op_sel_hi:[1,0]
	s_nop 0
	v_pk_mul_f32 v[30:31], v[42:43], v[52:53] op_sel_hi:[1,0]
	v_pk_mul_f32 v[28:29], v[82:83], v[52:53] op_sel_hi:[1,0]
	s_waitcnt vmcnt(1)
	v_pk_mul_f32 v[30:31], v[34:35], v[30:31]
	v_pk_mul_f32 v[28:29], v[32:33], v[28:29]
	global_store_dwordx4 v[10:11], v[28:31], off offset:-2032 nt
	global_load_dwordx4 v[28:31], v[2:3], off
	s_nop 0
	global_load_dwordx4 v[32:35], v[2:3], off offset:16
	v_pk_mul_f32 v[42:43], v[88:89], v[52:53] op_sel_hi:[1,0]
	s_waitcnt vmcnt(1)
	v_pk_mul_f32 v[28:29], v[28:29], v[40:41]
	v_pk_mul_f32 v[30:31], v[30:31], v[36:37]
	s_waitcnt vmcnt(0)
	v_pk_mul_f32 v[32:33], v[32:33], v[42:43]
	v_pk_mul_f32 v[34:35], v[34:35], v[38:39]
	global_store_dwordx4 v[10:11], v[28:31], off nt
	global_store_dwordx4 v[10:11], v[32:35], off offset:16 nt
	global_load_dwordx4 v[28:31], v[4:5], off
	s_nop 0
	global_load_dwordx4 v[32:35], v[4:5], off offset:16
	v_pk_mul_f32 v[36:37], v[92:93], v[52:53] op_sel_hi:[1,0]
	v_pk_mul_f32 v[38:39], v[64:65], v[52:53] op_sel_hi:[1,0]
	v_pk_mul_f32 v[40:41], v[94:95], v[52:53] op_sel_hi:[1,0]
	s_waitcnt vmcnt(1)
	v_pk_mul_f32 v[28:29], v[28:29], v[38:39]
	v_pk_mul_f32 v[30:31], v[30:31], v[36:37]
	s_waitcnt vmcnt(0)
	v_pk_mul_f32 v[32:33], v[32:33], v[40:41]
	v_pk_mul_f32 v[34:35], v[34:35], v[14:15]
	global_store_dwordx4 v[10:11], v[28:31], off offset:2048 nt
	global_store_dwordx4 v[10:11], v[32:35], off offset:2064 nt
	v_lshl_add_u64 v[10:11], v[10:11], 0, s[10:11]
	s_cbranch_scc0 .LBB0_789
